# default-policy SwiGLU activation stores plus nt policy on the final output stores
# speedup vs baseline: 1.0075x; 1.0009x over previous
; #define GAS __attribute__((address_space(1)))
; __device__ __forceinline__ float bf_lo(unsigned w) { return __uint_as_float(w << 16); }
; __device__ __forceinline__ float bf_hi(unsigned w) { return __uint_as_float(w & 0xffff0000u); }
; __device__ __forceinline__ void final_rows(Frame& F, const bf16* XA, const bf16* YS, const int* posi, const float* wl, const float* PART, const LAS int* tab, const float* gate, const float* g, float* out) {
;     ...
;             f32x4 v[4]; float s = 0.f;
; #pragma unroll
;             for (int j = 0; j < 4; ++j) { const unsigned long long xq = xr[64 * j]; const unsigned xl = (unsigned)xq, xh = (unsigned)(xq >> 32);
;                 v[j] = (f32x4){bf_lo(xl), bf_hi(xl), bf_lo(xh), bf_hi(xh)} + gt[j] * ys[j]; s += (v[j].x * v[j].x + v[j].y * v[j].y) + (v[j].z * v[j].z + v[j].w * v[j].w); }
;             const float rstd = rsqrtf(wave_sum(s) * (1.f / D) + RMS_EPS);
;             GAS f32x4* o = (GAS f32x4*)(out + (size_t)row * D) + lane;
; #pragma unroll
;             for (int j = 0; j < 4; ++j) o[64 * j] = v[j] * rstd * gf[j];
.LBB0_1948:
	s_ashr_i32 s3, s2, 31
	s_lshl_b64 s[4:5], s[2:3], 11
	v_lshl_add_u64 v[12:13], v[54:55], 0, s[4:5]
	global_load_dwordx2 v[14:15], v[12:13], off
	global_load_dwordx2 v[64:65], v[12:13], off offset:512
	global_load_dwordx2 v[66:67], v[12:13], off offset:1024
	global_load_dwordx2 v[68:69], v[12:13], off offset:1536
	s_add_i32 s26, s26, 2
	s_lshl_b64 s[2:3], s[2:3], 12
	s_cmp_eq_u32 s26, 8
	s_waitcnt vmcnt(3)
	v_lshlrev_b32_e32 v12, 16, v14
	v_and_b32_e32 v13, 0xffff0000, v14
	v_lshlrev_b32_e32 v14, 16, v15
	v_and_b32_e32 v15, 0xffff0000, v15
	s_waitcnt vmcnt(2)
	v_lshlrev_b32_e32 v70, 16, v64
	v_and_b32_e32 v71, 0xffff0000, v64
	v_lshlrev_b32_e32 v64, 16, v65
	v_and_b32_e32 v65, 0xffff0000, v65
	s_waitcnt vmcnt(1)
	v_lshlrev_b32_e32 v72, 16, v66
	v_and_b32_e32 v73, 0xffff0000, v66
	v_lshlrev_b32_e32 v66, 16, v67
	v_and_b32_e32 v67, 0xffff0000, v67
	s_waitcnt vmcnt(0)
	v_lshlrev_b32_e32 v76, 16, v68
	v_and_b32_e32 v77, 0xffff0000, v68
	v_lshlrev_b32_e32 v68, 16, v69
	v_and_b32_e32 v69, 0xffff0000, v69
	v_pk_fma_f32 v[0:1], v[16:17], v[0:1], v[12:13]
	v_pk_fma_f32 v[2:3], v[18:19], v[2:3], v[14:15]
	v_pk_fma_f32 v[4:5], v[20:21], v[4:5], v[70:71]
	v_pk_fma_f32 v[6:7], v[22:23], v[6:7], v[64:65]
	v_pk_fma_f32 v[10:11], v[34:35], v[10:11], v[66:67]
	v_pk_fma_f32 v[12:13], v[38:39], v[50:51], v[68:69]
	v_pk_fma_f32 v[14:15], v[36:37], v[48:49], v[76:77]
	v_pk_mul_f32 v[48:49], v[2:3], v[2:3]
	v_pk_mul_f32 v[50:51], v[0:1], v[0:1]
	v_pk_mul_f32 v[64:65], v[6:7], v[6:7]
	v_pk_mul_f32 v[66:67], v[4:5], v[4:5]
	v_pk_fma_f32 v[8:9], v[32:33], v[8:9], v[72:73]
	v_pk_mov_b32 v[72:73], v[50:51], v[48:49] op_sel:[1,0]
	v_mov_b32_e32 v51, v49
	v_pk_mov_b32 v[48:49], v[66:67], v[64:65] op_sel:[1,0]
	v_mov_b32_e32 v67, v65
	v_mul_f32_e32 v71, v14, v14
	v_mul_f32_e32 v68, v9, v9
	v_mul_f32_e32 v70, v11, v11
	v_pk_add_f32 v[50:51], v[72:73], v[50:51]
	v_pk_add_f32 v[48:49], v[48:49], v[66:67]
	v_mul_f32_e32 v74, v15, v15
	v_mul_f32_e32 v76, v12, v12
	v_mul_f32_e32 v77, v13, v13
	v_pk_fma_f32 v[64:65], v[8:9], v[8:9], v[68:69] op_sel_hi:[1,1,0]
	v_pk_fma_f32 v[68:69], v[10:11], v[10:11], v[70:71] op_sel_hi:[1,1,0]
	v_pk_add_f32 v[50:51], v[50:51], v[50:51] op_sel:[0,1] op_sel_hi:[1,0]
	v_pk_add_f32 v[48:49], v[48:49], v[48:49] op_sel:[0,1] op_sel_hi:[1,0]
	v_mov_b32_e32 v65, v76
	v_mov_b32_e32 v69, v77
	v_mov_b32_e32 v51, v71
	v_mov_b32_e32 v49, v74
	v_pk_add_f32 v[64:65], v[64:65], v[68:69]
	v_pk_add_f32 v[48:49], v[50:51], v[48:49]
	s_nop 0
	v_pk_add_f32 v[48:49], v[48:49], v[64:65]
	s_nop 0
	v_add_f32_e32 v48, v48, v49
	ds_bpermute_b32 v49, v75, v48
	s_waitcnt lgkmcnt(0)
	v_add_f32_e32 v48, v48, v49
	ds_bpermute_b32 v49, v78, v48
	s_waitcnt lgkmcnt(0)
	v_add_f32_e32 v48, v48, v49
	ds_bpermute_b32 v49, v79, v48
	s_waitcnt lgkmcnt(0)
	v_add_f32_e32 v48, v48, v49
	ds_bpermute_b32 v49, v80, v48
	s_waitcnt lgkmcnt(0)
	v_add_f32_e32 v48, v48, v49
	ds_bpermute_b32 v49, v81, v48
	s_waitcnt lgkmcnt(0)
	v_add_f32_e32 v48, v48, v49
	ds_bpermute_b32 v49, v82, v48
	s_waitcnt lgkmcnt(0)
	v_add_f32_e32 v48, v48, v49
	v_fmamk_f32 v48, v48, 0x3a800000, v85
	v_mul_f32_e32 v49, 0x4b800000, v48
	v_cmp_gt_f32_e32 vcc, s19, v48
	s_nop 1
	v_cndmask_b32_e32 v48, v48, v49, vcc
	v_rsq_f32_e32 v50, v48
	v_lshl_add_u64 v[48:49], v[60:61], 0, s[2:3]
	v_mul_f32_e32 v51, 0x45800000, v50
	v_cndmask_b32_e32 v50, v50, v51, vcc
	v_pk_mul_f32 v[0:1], v[0:1], v[50:51] op_sel_hi:[1,0]
	v_pk_mul_f32 v[2:3], v[2:3], v[50:51] op_sel_hi:[1,0]
	v_pk_mul_f32 v[4:5], v[4:5], v[50:51] op_sel_hi:[1,0]
	v_pk_mul_f32 v[6:7], v[6:7], v[50:51] op_sel_hi:[1,0]
	v_pk_mul_f32 v[8:9], v[8:9], v[50:51] op_sel_hi:[1,0]
	v_pk_mul_f32 v[10:11], v[10:11], v[50:51] op_sel_hi:[1,0]
	v_pk_mul_f32 v[64:65], v[14:15], v[50:51] op_sel_hi:[1,0]
	v_pk_mul_f32 v[12:13], v[12:13], v[50:51] op_sel_hi:[1,0]
	v_pk_mul_f32 v[2:3], v[26:27], v[2:3]
	v_pk_mul_f32 v[0:1], v[24:25], v[0:1]
	v_pk_mul_f32 v[6:7], v[30:31], v[6:7]
	v_pk_mul_f32 v[4:5], v[28:29], v[4:5]
	v_pk_mul_f32 v[10:11], v[42:43], v[10:11]
	v_pk_mul_f32 v[8:9], v[40:41], v[8:9]
	v_pk_mul_f32 v[14:15], v[46:47], v[12:13]
	v_pk_mul_f32 v[12:13], v[44:45], v[64:65]
	global_store_dwordx4 v[48:49], v[0:3], off nt
	global_store_dwordx4 v[48:49], v[4:7], off offset:1024 nt
	global_store_dwordx4 v[48:49], v[8:11], off offset:2048 nt
	global_store_dwordx4 v[48:49], v[12:15], off offset:3072 nt
	s_cbranch_scc1 .LBB0_1946

; #define GAS __attribute__((address_space(1)))
; __device__ __forceinline__ float bf_lo(unsigned w) { return __uint_as_float(w << 16); }
; __device__ __forceinline__ float bf_hi(unsigned w) { return __uint_as_float(w & 0xffff0000u); }
; __device__ __forceinline__ void final_rows(Frame& F, const bf16* XA, const bf16* YS, const int* posi, const float* wl, const float* PART, const LAS int* tab, const float* gate, const float* g, float* out) {
;     ...
;             const int row = row0 + r;
;             const GAS unsigned long long* xr = (const GAS unsigned long long*)(XA + (size_t)row * D) + lane;
;             const int d0 = __builtin_amdgcn_readfirstlane(posi[2 * row]), d1 = __builtin_amdgcn_readfirstlane(posi[2 * row + 1]);
;             const float w0 = __builtin_bit_cast(float, __builtin_amdgcn_readfirstlane(__builtin_bit_cast(int, wl[d0]))), w1 = __builtin_bit_cast(float, __builtin_amdgcn_readfirstlane(__builtin_bit_cast(int, wl[d1])));
;             const int c0 = __builtin_amdgcn_readfirstlane(tab[d0 >> 14]) * 256 + (d0 & (ECAP - 1)), c1 = __builtin_amdgcn_readfirstlane(tab[d1 >> 14]) * 256 + (d1 & (ECAP - 1));
;             f32x4 ys[4];
;             if (c0 < pg8::TAIL_M0 * 256 && c1 < pg8::TAIL_M0 * 256) {
;     ...
;             f32x4 v[4]; float s = 0.f;
; #pragma unroll
;             for (int j = 0; j < 4; ++j) { const unsigned long long xq = xr[64 * j]; const unsigned xl = (unsigned)xq, xh = (unsigned)(xq >> 32);
;                 v[j] = (f32x4){bf_lo(xl), bf_hi(xl), bf_lo(xh), bf_hi(xh)} + gt[j] * ys[j]; s += (v[j].x * v[j].x + v[j].y * v[j].y) + (v[j].z * v[j].z + v[j].w * v[j].w); }
;             const float rstd = rsqrtf(wave_sum(s) * (1.f / D) + RMS_EPS);
;             GAS f32x4* o = (GAS f32x4*)(out + (size_t)row * D) + lane;
; #pragma unroll
;             for (int j = 0; j < 4; ++j) o[64 * j] = v[j] * rstd * gf[j];
.LBB0_1959:
	s_ashr_i32 s5, s4, 31
	s_lshl_b64 s[2:3], s[4:5], 11
	v_lshl_add_u64 v[12:13], v[54:55], 0, s[2:3]
	global_load_dwordx2 v[14:15], v[12:13], off
	global_load_dwordx2 v[64:65], v[12:13], off offset:512
	global_load_dwordx2 v[66:67], v[12:13], off offset:1024
	global_load_dwordx2 v[68:69], v[12:13], off offset:1536
	s_add_i32 s2, s4, 1
	s_lshl_b32 s8, s2, 1
	s_lshl_b64 s[4:5], s[4:5], 12
	s_ashr_i32 s9, s8, 31
	s_waitcnt vmcnt(3)
	v_lshlrev_b32_e32 v12, 16, v14
	v_and_b32_e32 v13, 0xffff0000, v14
	v_lshlrev_b32_e32 v14, 16, v15
	v_and_b32_e32 v15, 0xffff0000, v15
	s_waitcnt vmcnt(2)
	v_lshlrev_b32_e32 v70, 16, v64
	v_and_b32_e32 v71, 0xffff0000, v64
	v_lshlrev_b32_e32 v64, 16, v65
	v_and_b32_e32 v65, 0xffff0000, v65
	s_waitcnt vmcnt(1)
	v_lshlrev_b32_e32 v72, 16, v66
	v_and_b32_e32 v73, 0xffff0000, v66
	v_lshlrev_b32_e32 v66, 16, v67
	v_and_b32_e32 v67, 0xffff0000, v67
	s_waitcnt vmcnt(0)
	v_lshlrev_b32_e32 v76, 16, v68
	v_and_b32_e32 v77, 0xffff0000, v68
	v_lshlrev_b32_e32 v68, 16, v69
	v_and_b32_e32 v69, 0xffff0000, v69
	v_pk_fma_f32 v[0:1], v[16:17], v[0:1], v[12:13]
	v_pk_fma_f32 v[2:3], v[18:19], v[2:3], v[14:15]
	v_pk_fma_f32 v[4:5], v[20:21], v[4:5], v[70:71]
	v_pk_fma_f32 v[6:7], v[22:23], v[6:7], v[64:65]
	v_pk_fma_f32 v[10:11], v[34:35], v[10:11], v[66:67]
	v_pk_fma_f32 v[12:13], v[38:39], v[50:51], v[68:69]
	v_pk_fma_f32 v[14:15], v[36:37], v[48:49], v[76:77]
	v_pk_mul_f32 v[48:49], v[2:3], v[2:3]
	v_pk_mul_f32 v[50:51], v[0:1], v[0:1]
	v_pk_mul_f32 v[64:65], v[6:7], v[6:7]
	v_pk_mul_f32 v[66:67], v[4:5], v[4:5]
	v_pk_fma_f32 v[8:9], v[32:33], v[8:9], v[72:73]
	v_pk_mov_b32 v[72:73], v[50:51], v[48:49] op_sel:[1,0]
	v_mov_b32_e32 v51, v49
	v_pk_mov_b32 v[48:49], v[66:67], v[64:65] op_sel:[1,0]
	v_mov_b32_e32 v67, v65
	v_mul_f32_e32 v71, v14, v14
	v_mul_f32_e32 v68, v9, v9
	v_mul_f32_e32 v70, v11, v11
	v_pk_add_f32 v[50:51], v[72:73], v[50:51]
	v_pk_add_f32 v[48:49], v[48:49], v[66:67]
	v_mul_f32_e32 v74, v15, v15
	v_mul_f32_e32 v76, v12, v12
	v_mul_f32_e32 v77, v13, v13
	v_pk_fma_f32 v[64:65], v[8:9], v[8:9], v[68:69] op_sel_hi:[1,1,0]
	v_pk_fma_f32 v[68:69], v[10:11], v[10:11], v[70:71] op_sel_hi:[1,1,0]
	v_pk_add_f32 v[50:51], v[50:51], v[50:51] op_sel:[0,1] op_sel_hi:[1,0]
	v_pk_add_f32 v[48:49], v[48:49], v[48:49] op_sel:[0,1] op_sel_hi:[1,0]
	v_mov_b32_e32 v65, v76
	v_mov_b32_e32 v69, v77
	v_mov_b32_e32 v51, v71
	v_mov_b32_e32 v49, v74
	v_pk_add_f32 v[64:65], v[64:65], v[68:69]
	v_pk_add_f32 v[48:49], v[50:51], v[48:49]
	s_nop 0
	v_pk_add_f32 v[48:49], v[48:49], v[64:65]
	s_nop 0
	v_add_f32_e32 v48, v48, v49
	ds_bpermute_b32 v49, v75, v48
	s_waitcnt lgkmcnt(0)
	v_add_f32_e32 v48, v48, v49
	ds_bpermute_b32 v49, v78, v48
	s_waitcnt lgkmcnt(0)
	v_add_f32_e32 v48, v48, v49
	ds_bpermute_b32 v49, v79, v48
	s_waitcnt lgkmcnt(0)
	v_add_f32_e32 v48, v48, v49
	ds_bpermute_b32 v49, v80, v48
	s_waitcnt lgkmcnt(0)
	v_add_f32_e32 v48, v48, v49
	ds_bpermute_b32 v49, v81, v48
	s_waitcnt lgkmcnt(0)
	v_add_f32_e32 v50, v48, v49
	ds_bpermute_b32 v51, v82, v50
	v_lshl_add_u64 v[48:49], v[60:61], 0, s[4:5]
	s_lshl_b64 s[4:5], s[8:9], 2
	s_add_u32 s4, s20, s4
	s_addc_u32 s5, s21, s5
	s_waitcnt lgkmcnt(0)
	v_add_f32_e32 v50, v50, v51
	v_fmamk_f32 v50, v50, 0x3a800000, v85
	v_mul_f32_e32 v51, 0x4b800000, v50
	v_cmp_gt_f32_e32 vcc, s19, v50
	s_nop 1
	v_cndmask_b32_e32 v50, v50, v51, vcc
	v_rsq_f32_e32 v50, v50
	s_nop 0
	v_mul_f32_e32 v51, 0x45800000, v50
	v_cndmask_b32_e32 v50, v50, v51, vcc
	v_pk_mul_f32 v[0:1], v[0:1], v[50:51] op_sel_hi:[1,0]
	v_pk_mul_f32 v[2:3], v[2:3], v[50:51] op_sel_hi:[1,0]
	v_pk_mul_f32 v[4:5], v[4:5], v[50:51] op_sel_hi:[1,0]
	v_pk_mul_f32 v[6:7], v[6:7], v[50:51] op_sel_hi:[1,0]
	v_pk_mul_f32 v[8:9], v[8:9], v[50:51] op_sel_hi:[1,0]
	v_pk_mul_f32 v[10:11], v[10:11], v[50:51] op_sel_hi:[1,0]
	v_pk_mul_f32 v[64:65], v[14:15], v[50:51] op_sel_hi:[1,0]
	v_pk_mul_f32 v[12:13], v[12:13], v[50:51] op_sel_hi:[1,0]
	v_pk_mul_f32 v[2:3], v[26:27], v[2:3]
	v_pk_mul_f32 v[0:1], v[24:25], v[0:1]
	v_pk_mul_f32 v[6:7], v[30:31], v[6:7]
	v_pk_mul_f32 v[4:5], v[28:29], v[4:5]
	v_pk_mul_f32 v[10:11], v[42:43], v[10:11]
	v_pk_mul_f32 v[8:9], v[40:41], v[8:9]
	v_pk_mul_f32 v[14:15], v[46:47], v[12:13]
	v_pk_mul_f32 v[12:13], v[44:45], v[64:65]
	global_store_dwordx4 v[48:49], v[0:3], off nt
	global_store_dwordx4 v[48:49], v[4:7], off offset:1024 nt
	global_store_dwordx4 v[48:49], v[8:11], off offset:2048 nt
	global_store_dwordx4 v[48:49], v[12:15], off offset:3072 nt
	global_load_dwordx2 v[0:1], v84, s[4:5]
	s_waitcnt vmcnt(0)
	v_readfirstlane_b32 s4, v0
	s_ashr_i32 s5, s4, 31
	s_lshl_b64 s[10:11], s[4:5], 2
	v_readfirstlane_b32 s8, v1
	s_add_u32 s10, s22, s10
	s_addc_u32 s11, s23, s11
	s_ashr_i32 s9, s8, 31
	s_lshl_b64 s[12:13], s[8:9], 2
	s_add_u32 s12, s22, s12
	s_addc_u32 s13, s23, s13
	global_load_dword v0, v84, s[10:11]
	global_load_dword v1, v84, s[12:13]
	s_ashr_i32 s0, s4, 14
	s_ashr_i32 s3, s8, 14
	s_lshl_b32 s0, s0, 2
	s_lshl_b32 s3, s3, 2
	s_add_i32 s0, s18, s0
	s_add_i32 s3, s18, s3
	v_mov_b32_e32 v2, s0
	v_mov_b32_e32 v3, s3
	ds_read_b32 v2, v2
	ds_read_b32 v3, v3
	s_and_b32 s0, s4, 0x3fff
	s_and_b32 s3, s8, 0x3fff
	s_mov_b64 s[12:13], -1
	s_waitcnt lgkmcnt(1)
	v_readfirstlane_b32 s4, v2
	s_waitcnt lgkmcnt(0)
	v_readfirstlane_b32 s5, v3
	s_lshl_b32 s4, s4, 8
	s_lshl_b32 s5, s5, 8
	s_add_i32 s10, s4, s0
	s_add_i32 s8, s5, s3
	s_max_i32 s0, s10, s8
	s_cmp_lt_i32 s0, 0x8000
	s_waitcnt vmcnt(1)
	v_readfirstlane_b32 s4, v0
	s_waitcnt vmcnt(0)
	v_readfirstlane_b32 s6, v1
	s_cbranch_scc1 .LBB0_1967
	v_mov_b32_e32 v48, 0
	v_mov_b32_e32 v49, v48
	v_mov_b32_e32 v50, v48
	v_mov_b32_e32 v51, v48
	v_mov_b32_e32 v0, v48
	v_mov_b32_e32 v1, v48
	v_mov_b32_e32 v64, v48
	v_mov_b32_e32 v65, v48
	v_mov_b32_e32 v66, v48
	v_mov_b32_e32 v67, v48
	v_mov_b32_e32 v68, v48
	v_mov_b32_e32 v69, v48
	v_mov_b32_e32 v70, v48
	v_mov_b32_e32 v71, v48
	v_mov_b32_e32 v72, v48
	v_mov_b32_e32 v73, v48
